# speedup vs baseline: 1.0281x; 1.0053x over previous
.Lk_15:
	global_load_dword v66, v[62:63], off offset:4
	global_load_dword v67, v[62:63], off offset:260
	global_load_dword v68, v[62:63], off offset:516
	global_load_dword v69, v[62:63], off offset:772
	global_load_dword v70, v[64:65], off offset:4
	global_load_dword v71, v[64:65], off offset:260
	global_load_dword v72, v[64:65], off offset:516
	global_load_dword v73, v[64:65], off offset:772
	v_and_b32_e32 v62, 15, v0
	s_mov_b32 s8, 0x4038aa3b
	s_waitcnt vmcnt(11)
	v_pk_mul_f32 v[38:39], v[50:51], v[38:39]
	v_lshlrev_b32_e32 v57, 2, v1
	s_lshl_b32 s10, s34, 8
	v_lshlrev_b32_e32 v1, 4, v62
	v_pk_add_f32 v[52:53], v[52:53], v[54:55]
	v_pk_add_f32 v[54:55], v[58:59], v[60:61]
	s_mov_b32 s9, 0xbfb8aa3b
	s_waitcnt vmcnt(10)
	v_pk_mul_f32 v[46:47], v[50:51], v[46:47]
	v_pk_mul_f32 v[48:49], v[50:51], v[48:49]
	v_pk_mul_f32 v[40:41], v[50:51], v[40:41]
	s_waitcnt vmcnt(8)
	v_pk_mul_f32 v[42:43], v[50:51], v[42:43]
	v_pk_mul_f32 v[44:45], v[50:51], v[44:45]
	v_pk_mul_f32 v[34:35], v[50:51], v[34:35]
	v_pk_mul_f32 v[36:37], v[50:51], v[36:37]
	v_pk_mul_f32 v[30:31], v[50:51], v[30:31]
	v_pk_mul_f32 v[32:33], v[50:51], v[32:33]
	v_pk_mul_f32 v[18:19], v[50:51], v[18:19]
	v_pk_mul_f32 v[58:59], v[50:51], v[20:21]
	v_pk_mul_f32 v[60:61], v[50:51], v[26:27]
	v_pk_mul_f32 v[64:65], v[50:51], v[28:29]
	v_pk_mul_f32 v[74:75], v[50:51], v[22:23]
	v_pk_mul_f32 v[50:51], v[50:51], v[24:25]
	v_cvt_pk_f16_f32 v24, v38, v39
	v_or3_b32 v38, v1, v57, s10
	v_lshlrev_b32_e32 v82, 4, v80
	s_and_b64 vcc, exec, s[6:7]
	s_mov_b32 s6, s9
	v_cvt_pk_f16_f32 v25, v40, v41
	v_add_u32_e32 v81, 0x23280, v38
	s_mov_b64 s[4:5], -1
	v_pk_mul_f32 v[20:21], v[54:55], s[8:9]
	v_cvt_pk_f16_f32 v22, v46, v47
	v_cvt_pk_f16_f32 v23, v48, v49
	v_cvt_pk_f16_f32 v26, v42, v43
	v_cvt_pk_f16_f32 v27, v44, v45
	v_cvt_pk_f16_f32 v28, v34, v35
	v_cvt_pk_f16_f32 v29, v36, v37
	v_cvt_pk_f16_f32 v30, v30, v31
	v_cvt_pk_f16_f32 v31, v32, v33
	v_cvt_pk_f16_f32 v32, v18, v19
	v_cvt_pk_f16_f32 v33, v58, v59
	v_cvt_pk_f16_f32 v34, v60, v61
	v_cvt_pk_f16_f32 v35, v64, v65
	v_cvt_pk_f16_f32 v36, v74, v75
	v_cvt_pk_f16_f32 v37, v50, v51
	v_add_u32_e32 v75, 0x23280, v82
	v_pk_mul_f32 v[18:19], v[52:53], s[6:7] op_sel_hi:[1,0]
	s_waitcnt lgkmcnt(0)
	s_barrier
	s_waitcnt vmcnt(2)
	v_pk_add_f32 v[38:39], v[66:67], v[70:71]
	s_nop 0
	v_pk_mul_f32 v[38:39], v[38:39], s[6:7] op_sel_hi:[1,0]
	s_waitcnt vmcnt(0)
	v_pk_add_f32 v[40:41], v[68:69], v[72:73]
	s_nop 0
	v_pk_mul_f32 v[40:41], v[40:41], s[8:9]
	s_cbranch_vccz .Lk_134
	s_setprio 0
	v_lshrrev_b32_e32 v42, 4, v80
	v_lshlrev_b32_e32 v42, 5, v42
	global_load_dwordx4 v[44:47], v42, s[18:19]
	global_load_dwordx4 v[48:51], v42, s[18:19] offset:16
	global_load_dwordx4 v[52:55], v42, s[18:19] offset:128
	global_load_dwordx4 v[56:59], v42, s[18:19] offset:144
	s_load_dword s28, s[20:21], 0x0
	v_and_b32_e32 v43, 15, v80
	v_cmp_eq_u32_e32 vcc, 1, v43
	v_cmp_eq_u32_e64 s[4:5], 0, v43
	v_cmp_gt_u32_e64 s[30:31], 16, v80
	v_lshl_or_b32 v124, s3, 4, v43
	v_mul_u32_u24_e32 v124, 0x708, v124
	v_lshlrev_b32_e32 v74, 2, v43
	v_add_u32_e32 v74, 0x1c200, v74
	v_mov_b32_e32 v72, 0x3fe10966
	v_mov_b32_e32 v73, 0xbfe10966
	v_mov_b32_e32 v92, 0xc038aa3b
	v_mov_b32_e32 v93, 0xc038aa3b
	s_mov_b32 s8, 0x4038aa3b
	s_mov_b32 s9, 0
	v_mov_b32_e32 v64, 0
	v_mov_b32_e32 v65, 0
	s_mov_b32 s12, 4
	s_waitcnt vmcnt(0) lgkmcnt(0)
	v_cvt_f16_f32_e32 v60, v44
	v_cvt_f32_f16_e32 v61, v60
	v_sub_f32_e32 v61, v44, v61
	v_cvt_f16_f32_e32 v61, v61
	v_cndmask_b32_e32 v61, 0, v61, vcc
	v_cndmask_b32_e64 v94, v61, v60, s[4:5]
	v_cvt_f16_f32_e32 v60, v45
	v_cvt_f32_f16_e32 v61, v60
	v_sub_f32_e32 v61, v45, v61
	v_cvt_f16_f32_e32 v61, v61
	v_cndmask_b32_e32 v61, 0, v61, vcc
	v_cndmask_b32_e64 v95, v61, v60, s[4:5]
	v_cvt_f16_f32_e32 v60, v46
	v_cvt_f32_f16_e32 v61, v60
	v_sub_f32_e32 v61, v46, v61
	v_cvt_f16_f32_e32 v61, v61
	v_cndmask_b32_e32 v61, 0, v61, vcc
	v_cndmask_b32_e64 v96, v61, v60, s[4:5]
	v_cvt_f16_f32_e32 v60, v47
	v_cvt_f32_f16_e32 v61, v60
	v_sub_f32_e32 v61, v47, v61
	v_cvt_f16_f32_e32 v61, v61
	v_cndmask_b32_e32 v61, 0, v61, vcc
	v_cndmask_b32_e64 v97, v61, v60, s[4:5]
	v_cvt_f16_f32_e32 v60, v48
	v_cvt_f32_f16_e32 v61, v60
	v_sub_f32_e32 v61, v48, v61
	v_cvt_f16_f32_e32 v61, v61
	v_cndmask_b32_e32 v61, 0, v61, vcc
	v_cndmask_b32_e64 v98, v61, v60, s[4:5]
	v_cvt_f16_f32_e32 v60, v49
	v_cvt_f32_f16_e32 v61, v60
	v_sub_f32_e32 v61, v49, v61
	v_cvt_f16_f32_e32 v61, v61
	v_cndmask_b32_e32 v61, 0, v61, vcc
	v_cndmask_b32_e64 v99, v61, v60, s[4:5]
	v_cvt_f16_f32_e32 v60, v50
	v_cvt_f32_f16_e32 v61, v60
	v_sub_f32_e32 v61, v50, v61
	v_cvt_f16_f32_e32 v61, v61
	v_cndmask_b32_e32 v61, 0, v61, vcc
	v_cndmask_b32_e64 v100, v61, v60, s[4:5]
	v_cvt_f16_f32_e32 v60, v51
	v_cvt_f32_f16_e32 v61, v60
	v_sub_f32_e32 v61, v51, v61
	v_cvt_f16_f32_e32 v61, v61
	v_cndmask_b32_e32 v61, 0, v61, vcc
	v_cndmask_b32_e64 v101, v61, v60, s[4:5]
	v_cvt_f16_f32_e32 v60, v52
	v_cvt_f32_f16_e32 v61, v60
	v_sub_f32_e32 v61, v52, v61
	v_cvt_f16_f32_e32 v61, v61
	v_cndmask_b32_e32 v61, 0, v61, vcc
	v_cndmask_b32_e64 v102, v61, v60, s[4:5]
	v_cvt_f16_f32_e32 v60, v53
	v_cvt_f32_f16_e32 v61, v60
	v_sub_f32_e32 v61, v53, v61
	v_cvt_f16_f32_e32 v61, v61
	v_cndmask_b32_e32 v61, 0, v61, vcc
	v_cndmask_b32_e64 v103, v61, v60, s[4:5]
	v_cvt_f16_f32_e32 v60, v54
	v_cvt_f32_f16_e32 v61, v60
	v_sub_f32_e32 v61, v54, v61
	v_cvt_f16_f32_e32 v61, v61
	v_cndmask_b32_e32 v61, 0, v61, vcc
	v_cndmask_b32_e64 v104, v61, v60, s[4:5]
	v_cvt_f16_f32_e32 v60, v55
	v_cvt_f32_f16_e32 v61, v60
	v_sub_f32_e32 v61, v55, v61
	v_cvt_f16_f32_e32 v61, v61
	v_cndmask_b32_e32 v61, 0, v61, vcc
	v_cndmask_b32_e64 v105, v61, v60, s[4:5]
	v_cvt_f16_f32_e32 v60, v56
	v_cvt_f32_f16_e32 v61, v60
	v_sub_f32_e32 v61, v56, v61
	v_cvt_f16_f32_e32 v61, v61
	v_cndmask_b32_e32 v61, 0, v61, vcc
	v_cndmask_b32_e64 v106, v61, v60, s[4:5]
	v_cvt_f16_f32_e32 v60, v57
	v_cvt_f32_f16_e32 v61, v60
	v_sub_f32_e32 v61, v57, v61
	v_cvt_f16_f32_e32 v61, v61
	v_cndmask_b32_e32 v61, 0, v61, vcc
	v_cndmask_b32_e64 v107, v61, v60, s[4:5]
	v_cvt_f16_f32_e32 v60, v58
	v_cvt_f32_f16_e32 v61, v60
	v_sub_f32_e32 v61, v58, v61
	v_cvt_f16_f32_e32 v61, v61
	v_cndmask_b32_e32 v61, 0, v61, vcc
	v_cndmask_b32_e64 v108, v61, v60, s[4:5]
	v_cvt_f16_f32_e32 v60, v59
	v_cvt_f32_f16_e32 v61, v60
	v_sub_f32_e32 v61, v59, v61
	v_cvt_f16_f32_e32 v61, v61
	v_cndmask_b32_e32 v61, 0, v61, vcc
	v_cndmask_b32_e64 v109, v61, v60, s[4:5]
	v_pack_b32_f16 v116, v94, v95
	v_pack_b32_f16 v117, v96, v97
	v_pack_b32_f16 v118, v98, v99
	v_pack_b32_f16 v119, v100, v101
	v_pack_b32_f16 v120, v102, v103
	v_pack_b32_f16 v121, v104, v105
	v_pack_b32_f16 v122, v106, v107
	v_pack_b32_f16 v123, v108, v109
	s_barrier
	ds_read_b128 v[44:47], v75 offset:0
	ds_read_b128 v[68:71], v75 offset:1024
	s_waitcnt lgkmcnt(0)
	v_mfma_f32_16x16x32_f16 v[84:87], v[2:5], v[44:47], v[18:21]
	v_mfma_f32_16x16x32_f16 v[88:91], v[14:17], v[44:47], v[38:41]
	v_mfma_f32_16x16x32_f16 v[84:87], v[6:9], v[68:71], v[84:87]
	v_mfma_f32_16x16x32_f16 v[88:91], v[10:13], v[68:71], v[88:91]
	s_barrier
	ds_read_b128 v[56:59], v75 offset:6144
	ds_read_b128 v[60:63], v75 offset:7168
	ds_read_b128 v[44:47], v75 offset:2048
	ds_read_b128 v[68:71], v75 offset:3072
	s_waitcnt lgkmcnt(3)
	v_mfma_f32_16x16x32_f16 v[84:87], v[30:33], v[56:59], v[84:87]
	v_mfma_f32_16x16x32_f16 v[88:91], v[22:25], v[56:59], v[88:91]
	s_waitcnt lgkmcnt(2)
	v_mfma_f32_16x16x32_f16 v[84:87], v[34:37], v[60:63], v[84:87]
	v_mfma_f32_16x16x32_f16 v[88:91], v[26:29], v[60:63], v[88:91]
	s_nop 7
	v_exp_f32_e32 v94, v86
	v_exp_f32_e32 v95, v90
	v_exp_f32_e32 v96, v84
	v_exp_f32_e32 v97, v88
	v_exp_f32_e32 v98, v85
	v_exp_f32_e32 v99, v89
	v_pk_add_f32 v[100:101], v[94:95], 1.0 op_sel_hi:[1,0]
	v_pk_fma_f32 v[102:103], v[94:95], s[8:9], v[92:93] op_sel_hi:[1,0,0]
	v_pk_fma_f32 v[100:101], v[96:97], v[100:101], v[100:101]
	v_pk_fma_f32 v[104:105], v[100:101], v[98:99], v[100:101]
	v_rcp_f32_e32 v104, v104
	v_rcp_f32_e32 v105, v105
	v_pk_fma_f32 v[102:103], v[102:103], v[98:99], v[102:103]
	v_pk_fma_f32 v[102:103], v[64:65], v[100:101], v[102:103]
	v_exp_f32_e32 v106, v87
	v_pk_mul_f32 v[64:65], v[102:103], v[104:105]
	v_exp_f32_e32 v108, v64
	v_exp_f32_e32 v109, v65
	v_exp_f32_e32 v107, v91
	v_pk_add_f32 v[110:111], v[108:109], 1.0 op_sel_hi:[1,0]
	v_pk_fma_f32 v[110:111], v[110:111], v[106:107], v[110:111]
	v_rcp_f32_e32 v110, v110
	v_rcp_f32_e32 v111, v111
	v_pk_add_f32 v[112:113], v[108:109], -1.0 op_sel_hi:[1,0]
	v_pk_mul_f32 v[112:113], v[112:113], v[110:111]
	v_cvt_pk_f16_f32 v114, v112, v113
	ds_write_b32 v81, v114 offset:4096
	s_waitcnt lgkmcnt(1)
	v_mfma_f32_16x16x32_f16 v[84:87], v[2:5], v[44:47], v[18:21]
	v_mfma_f32_16x16x32_f16 v[88:91], v[14:17], v[44:47], v[38:41]
	v_mfma_f32_16x16x32_f16 v[84:87], v[6:9], v[68:71], v[84:87]
	v_mfma_f32_16x16x32_f16 v[88:91], v[10:13], v[68:71], v[88:91]
	s_waitcnt lgkmcnt(0)
	s_barrier
	ds_read_b128 v[56:59], v75 offset:4096
	ds_read_b128 v[60:63], v75 offset:5120
	ds_read_b128 v[44:47], v75 offset:0
	ds_read_b128 v[68:71], v75 offset:1024
	s_waitcnt lgkmcnt(3)
	v_mfma_f32_16x16x32_f16 v[84:87], v[30:33], v[56:59], v[84:87]
	v_mfma_f32_16x16x32_f16 v[88:91], v[22:25], v[56:59], v[88:91]
	s_waitcnt lgkmcnt(2)
	v_mfma_f32_16x16x32_f16 v[84:87], v[34:37], v[60:63], v[84:87]
	v_mfma_f32_16x16x32_f16 v[88:91], v[26:29], v[60:63], v[88:91]
	s_cmp_eq_u32 s34, 0
	s_cbranch_scc0 .Lcb_o1_1
	v_mfma_f32_16x16x32_f16 v[50:53], v[116:119], v[56:59], 0
	s_branch .Lcb_o1s_2

.Lcb_o1s_2:
	s_nop 7
	v_exp_f32_e32 v94, v86
	v_exp_f32_e32 v95, v90
	v_exp_f32_e32 v96, v84
	v_exp_f32_e32 v97, v88
	v_exp_f32_e32 v98, v85
	v_exp_f32_e32 v99, v89
	s_cmp_lt_u32 s34, 2
	s_cbranch_scc0 .Lcb_o1h_3
	s_lshl_b32 s10, s34, 6
	s_cmp_eq_u32 s34, 0
	s_cselect_b32 s11, s28, 0
	v_add_f32_e32 v125, v50, v51
	v_add_f32_e32 v125, s11, v125
	v_add_u32_e32 v126, s10, v74
	s_mov_b64 s[16:17], exec
	s_mov_b64 exec, s[30:31]
	ds_write_b32 v126, v125 offset:128
	s_mov_b64 exec, s[16:17]
.Lcb_o1h_3:
	v_pk_add_f32 v[100:101], v[94:95], 1.0 op_sel_hi:[1,0]
	v_pk_fma_f32 v[102:103], v[94:95], s[8:9], v[92:93] op_sel_hi:[1,0,0]
	v_pk_fma_f32 v[100:101], v[96:97], v[100:101], v[100:101]
	v_pk_fma_f32 v[104:105], v[100:101], v[98:99], v[100:101]
	v_rcp_f32_e32 v104, v104
	v_rcp_f32_e32 v105, v105
	v_pk_fma_f32 v[102:103], v[102:103], v[98:99], v[102:103]
	v_pk_fma_f32 v[102:103], v[64:65], v[100:101], v[102:103]
	v_exp_f32_e32 v106, v87
	v_pk_mul_f32 v[64:65], v[102:103], v[104:105]
	v_exp_f32_e32 v108, v64
	v_exp_f32_e32 v109, v65
	v_exp_f32_e32 v107, v91
	v_pk_add_f32 v[110:111], v[108:109], 1.0 op_sel_hi:[1,0]
	v_pk_fma_f32 v[110:111], v[110:111], v[106:107], v[110:111]
	v_rcp_f32_e32 v110, v110
	v_rcp_f32_e32 v111, v111
	v_pk_add_f32 v[112:113], v[108:109], -1.0 op_sel_hi:[1,0]
	v_pk_mul_f32 v[112:113], v[112:113], v[110:111]
	v_cvt_pk_f16_f32 v114, v112, v113
	ds_write_b32 v81, v114 offset:6144
	s_waitcnt lgkmcnt(1)
	v_mfma_f32_16x16x32_f16 v[84:87], v[2:5], v[44:47], v[18:21]
	v_mfma_f32_16x16x32_f16 v[88:91], v[14:17], v[44:47], v[38:41]
	v_mfma_f32_16x16x32_f16 v[84:87], v[6:9], v[68:71], v[84:87]
	v_mfma_f32_16x16x32_f16 v[88:91], v[10:13], v[68:71], v[88:91]
	s_waitcnt lgkmcnt(0)
.Lcb_loop:
	s_barrier
	s_cmp_eq_u32 s34, 2
	s_cbranch_scc0 .Lcb_o2r_4
	ds_read_b32 v125, v74 offset:128
	ds_read_b32 v126, v74 offset:192
.Lcb_o2r_4:
	ds_read_b128 v[56:59], v75 offset:6144
	ds_read_b128 v[60:63], v75 offset:7168
	ds_read_b128 v[44:47], v75 offset:2048
	ds_read_b128 v[68:71], v75 offset:3072
	s_waitcnt lgkmcnt(3)
	v_mfma_f32_16x16x32_f16 v[84:87], v[30:33], v[56:59], v[84:87]
	v_mfma_f32_16x16x32_f16 v[88:91], v[22:25], v[56:59], v[88:91]
	s_waitcnt lgkmcnt(2)
	v_mfma_f32_16x16x32_f16 v[84:87], v[34:37], v[60:63], v[84:87]
	v_mfma_f32_16x16x32_f16 v[88:91], v[26:29], v[60:63], v[88:91]
	s_cmp_eq_u32 s34, 0
	s_cbranch_scc0 .Lcb_o1_5
	v_mfma_f32_16x16x32_f16 v[50:53], v[116:119], v[56:59], 0
	s_branch .Lcb_o1s_6

.Lcb_o1s_6:
	s_cmp_eq_u32 s34, 2
	s_cbranch_scc0 .Lcb_o2s_7
	v_add_f32_e32 v125, v125, v126
	v_mul_f32_e32 v126, 0x3fb8aa3b, v125
	v_exp_f32_e32 v126, v126
	v_cmp_lt_f32_e32 vcc, 0, v125
	v_mul_f32_e32 v125, 0x3f867d5f, v125
	v_fma_f32 v126, v126, v72, v73
	s_nop 0
	v_cndmask_b32_e32 v125, v126, v125, vcc
	s_mov_b64 s[16:17], exec
	s_mov_b64 exec, s[30:31]
	global_store_dword v124, v125, s[26:27] offset:0
	s_mov_b64 exec, s[16:17]
.Lcb_o2s_7:
	s_nop 7
	v_exp_f32_e32 v94, v86
	v_exp_f32_e32 v95, v90
	v_exp_f32_e32 v96, v84
	v_exp_f32_e32 v97, v88
	v_exp_f32_e32 v98, v85
	v_exp_f32_e32 v99, v89
	s_cmp_lt_u32 s34, 2
	s_cbranch_scc0 .Lcb_o1h_8
	s_lshl_b32 s10, s34, 6
	s_cmp_eq_u32 s34, 0
	s_cselect_b32 s11, s28, 0
	v_add_f32_e32 v125, v50, v51
	v_add_f32_e32 v125, s11, v125
	v_add_u32_e32 v126, s10, v74
	s_mov_b64 s[16:17], exec
	s_mov_b64 exec, s[30:31]
	ds_write_b32 v126, v125 offset:0
	s_mov_b64 exec, s[16:17]
.Lcb_o1h_8:
	v_pk_add_f32 v[100:101], v[94:95], 1.0 op_sel_hi:[1,0]
	v_pk_fma_f32 v[102:103], v[94:95], s[8:9], v[92:93] op_sel_hi:[1,0,0]
	v_pk_fma_f32 v[100:101], v[96:97], v[100:101], v[100:101]
	v_pk_fma_f32 v[104:105], v[100:101], v[98:99], v[100:101]
	v_rcp_f32_e32 v104, v104
	v_rcp_f32_e32 v105, v105
	v_pk_fma_f32 v[102:103], v[102:103], v[98:99], v[102:103]
	v_pk_fma_f32 v[102:103], v[64:65], v[100:101], v[102:103]
	v_exp_f32_e32 v106, v87
	v_pk_mul_f32 v[64:65], v[102:103], v[104:105]
	v_exp_f32_e32 v108, v64
	v_exp_f32_e32 v109, v65
	v_exp_f32_e32 v107, v91
	v_pk_add_f32 v[110:111], v[108:109], 1.0 op_sel_hi:[1,0]
	v_pk_fma_f32 v[110:111], v[110:111], v[106:107], v[110:111]
	v_rcp_f32_e32 v110, v110
	v_rcp_f32_e32 v111, v111
	v_pk_add_f32 v[112:113], v[108:109], -1.0 op_sel_hi:[1,0]
	v_pk_mul_f32 v[112:113], v[112:113], v[110:111]
	v_cvt_pk_f16_f32 v114, v112, v113
	ds_write_b32 v81, v114 offset:4096
	s_waitcnt lgkmcnt(1)
	v_mfma_f32_16x16x32_f16 v[84:87], v[2:5], v[44:47], v[18:21]
	v_mfma_f32_16x16x32_f16 v[88:91], v[14:17], v[44:47], v[38:41]
	v_mfma_f32_16x16x32_f16 v[84:87], v[6:9], v[68:71], v[84:87]
	v_mfma_f32_16x16x32_f16 v[88:91], v[10:13], v[68:71], v[88:91]
	s_waitcnt lgkmcnt(0)
	s_barrier
	s_cmp_eq_u32 s34, 2
	s_cbranch_scc0 .Lcb_o2r_9
	ds_read_b32 v125, v74 offset:0
	ds_read_b32 v126, v74 offset:64
.Lcb_o2r_9:
	ds_read_b128 v[56:59], v75 offset:4096
	ds_read_b128 v[60:63], v75 offset:5120
	ds_read_b128 v[44:47], v75 offset:0
	ds_read_b128 v[68:71], v75 offset:1024
	s_waitcnt lgkmcnt(3)
	v_mfma_f32_16x16x32_f16 v[84:87], v[30:33], v[56:59], v[84:87]
	v_mfma_f32_16x16x32_f16 v[88:91], v[22:25], v[56:59], v[88:91]
	s_waitcnt lgkmcnt(2)
	v_mfma_f32_16x16x32_f16 v[84:87], v[34:37], v[60:63], v[84:87]
	v_mfma_f32_16x16x32_f16 v[88:91], v[26:29], v[60:63], v[88:91]
	s_cmp_eq_u32 s34, 0
	s_cbranch_scc0 .Lcb_o1_10
	v_mfma_f32_16x16x32_f16 v[50:53], v[116:119], v[56:59], 0
	s_branch .Lcb_o1s_11

.Lcb_o1s_11:
	s_cmp_eq_u32 s34, 2
	s_cbranch_scc0 .Lcb_o2s_12
	v_add_f32_e32 v125, v125, v126
	v_mul_f32_e32 v126, 0x3fb8aa3b, v125
	v_exp_f32_e32 v126, v126
	v_cmp_lt_f32_e32 vcc, 0, v125
	v_mul_f32_e32 v125, 0x3f867d5f, v125
	v_fma_f32 v126, v126, v72, v73
	s_nop 0
	v_cndmask_b32_e32 v125, v126, v125, vcc
	s_mov_b64 s[16:17], exec
	s_mov_b64 exec, s[30:31]
	global_store_dword v124, v125, s[26:27] offset:4
	s_mov_b64 exec, s[16:17]

.Lcb_o1h_13:
	v_pk_add_f32 v[100:101], v[94:95], 1.0 op_sel_hi:[1,0]
	v_pk_fma_f32 v[102:103], v[94:95], s[8:9], v[92:93] op_sel_hi:[1,0,0]
	v_pk_fma_f32 v[100:101], v[96:97], v[100:101], v[100:101]
	v_pk_fma_f32 v[104:105], v[100:101], v[98:99], v[100:101]
	v_rcp_f32_e32 v104, v104
	v_rcp_f32_e32 v105, v105
	v_pk_fma_f32 v[102:103], v[102:103], v[98:99], v[102:103]
	v_pk_fma_f32 v[102:103], v[64:65], v[100:101], v[102:103]
	v_exp_f32_e32 v106, v87
	v_pk_mul_f32 v[64:65], v[102:103], v[104:105]
	v_exp_f32_e32 v108, v64
	v_exp_f32_e32 v109, v65
	v_exp_f32_e32 v107, v91
	v_pk_add_f32 v[110:111], v[108:109], 1.0 op_sel_hi:[1,0]
	v_pk_fma_f32 v[110:111], v[110:111], v[106:107], v[110:111]
	v_rcp_f32_e32 v110, v110
	v_rcp_f32_e32 v111, v111
	v_pk_add_f32 v[112:113], v[108:109], -1.0 op_sel_hi:[1,0]
	v_pk_mul_f32 v[112:113], v[112:113], v[110:111]
	v_cvt_pk_f16_f32 v114, v112, v113
	ds_write_b32 v81, v114 offset:6144
	s_waitcnt lgkmcnt(1)
	v_mfma_f32_16x16x32_f16 v[84:87], v[2:5], v[44:47], v[18:21]
	v_mfma_f32_16x16x32_f16 v[88:91], v[14:17], v[44:47], v[38:41]
	v_mfma_f32_16x16x32_f16 v[84:87], v[6:9], v[68:71], v[84:87]
	v_mfma_f32_16x16x32_f16 v[88:91], v[10:13], v[68:71], v[88:91]
	s_waitcnt lgkmcnt(0)
	s_barrier
	s_cmp_eq_u32 s34, 2
	s_cbranch_scc0 .Lcb_o2r_14
	ds_read_b32 v125, v74 offset:128
	ds_read_b32 v126, v74 offset:192

.Lcb_o1s_16:
	s_cmp_eq_u32 s34, 2
	s_cbranch_scc0 .Lcb_o2s_17
	v_add_f32_e32 v125, v125, v126
	v_mul_f32_e32 v126, 0x3fb8aa3b, v125
	v_exp_f32_e32 v126, v126
	v_cmp_lt_f32_e32 vcc, 0, v125
	v_mul_f32_e32 v125, 0x3f867d5f, v125
	v_fma_f32 v126, v126, v72, v73
	s_nop 0
	v_cndmask_b32_e32 v125, v126, v125, vcc
	s_mov_b64 s[16:17], exec
	s_mov_b64 exec, s[30:31]
	global_store_dword v124, v125, s[26:27] offset:8
	s_mov_b64 exec, s[16:17]

.Lcb_o1s_21:
	s_cmp_eq_u32 s34, 2
	s_cbranch_scc0 .Lcb_o2s_22
	v_add_f32_e32 v125, v125, v126
	v_mul_f32_e32 v126, 0x3fb8aa3b, v125
	v_exp_f32_e32 v126, v126
	v_cmp_lt_f32_e32 vcc, 0, v125
	v_mul_f32_e32 v125, 0x3f867d5f, v125
	v_fma_f32 v126, v126, v72, v73
	s_nop 0
	v_cndmask_b32_e32 v125, v126, v125, vcc
	s_mov_b64 s[16:17], exec
	s_mov_b64 exec, s[30:31]
	global_store_dword v124, v125, s[26:27] offset:12
	s_mov_b64 exec, s[16:17]

.Lcb_o1h_23:
	v_pk_add_f32 v[100:101], v[94:95], 1.0 op_sel_hi:[1,0]
	v_pk_fma_f32 v[102:103], v[94:95], s[8:9], v[92:93] op_sel_hi:[1,0,0]
	v_pk_fma_f32 v[100:101], v[96:97], v[100:101], v[100:101]
	v_pk_fma_f32 v[104:105], v[100:101], v[98:99], v[100:101]
	v_rcp_f32_e32 v104, v104
	v_rcp_f32_e32 v105, v105
	v_pk_fma_f32 v[102:103], v[102:103], v[98:99], v[102:103]
	v_pk_fma_f32 v[102:103], v[64:65], v[100:101], v[102:103]
	v_exp_f32_e32 v106, v87
	v_pk_mul_f32 v[64:65], v[102:103], v[104:105]
	v_exp_f32_e32 v108, v64
	v_exp_f32_e32 v109, v65
	v_exp_f32_e32 v107, v91
	v_pk_add_f32 v[110:111], v[108:109], 1.0 op_sel_hi:[1,0]
	v_pk_fma_f32 v[110:111], v[110:111], v[106:107], v[110:111]
	v_rcp_f32_e32 v110, v110
	v_rcp_f32_e32 v111, v111
	v_pk_add_f32 v[112:113], v[108:109], -1.0 op_sel_hi:[1,0]
	v_pk_mul_f32 v[112:113], v[112:113], v[110:111]
	v_cvt_pk_f16_f32 v114, v112, v113
	ds_write_b32 v81, v114 offset:6144
	s_waitcnt lgkmcnt(1)
	v_mfma_f32_16x16x32_f16 v[84:87], v[2:5], v[44:47], v[18:21]
	v_mfma_f32_16x16x32_f16 v[88:91], v[14:17], v[44:47], v[38:41]
	v_mfma_f32_16x16x32_f16 v[84:87], v[6:9], v[68:71], v[84:87]
	v_mfma_f32_16x16x32_f16 v[88:91], v[10:13], v[68:71], v[88:91]
	s_waitcnt lgkmcnt(0)
	v_min_f32_e32 v64, 0x42700000, v64
	v_min_f32_e32 v65, 0x42700000, v65
	s_add_u32 s12, s12, 4
	v_add_u32_e32 v124, 16, v124
	s_cmp_lt_u32 s12, 452
	s_cbranch_scc1 .Lcb_loop
	s_barrier
	s_cmp_eq_u32 s34, 2
	s_cbranch_scc0 .Lcb_o2r_24
	ds_read_b32 v125, v74 offset:128
	ds_read_b32 v126, v74 offset:192
.Lcb_o2r_24:
	ds_read_b128 v[56:59], v75 offset:6144
	ds_read_b128 v[60:63], v75 offset:7168
	s_waitcnt lgkmcnt(0)
	s_cmp_eq_u32 s34, 0
	s_cbranch_scc0 .Lcb_o1_25
	v_mfma_f32_16x16x32_f16 v[50:53], v[116:119], v[56:59], 0
	s_nop 7
	v_add_f32_e32 v125, v50, v51
	v_add_f32_e32 v125, s28, v125
	s_mov_b64 s[16:17], exec
	s_mov_b64 exec, s[30:31]
	ds_write_b32 v74, v125 offset:0
	s_mov_b64 exec, s[16:17]
	s_branch .Lcb_o1s_27

.Lcb_o2r_29:
	s_cmp_eq_u32 s34, 2
	s_cbranch_scc0 .Lcb_o2s_30
	s_waitcnt lgkmcnt(0)
	v_add_f32_e32 v125, v125, v126
	v_mul_f32_e32 v126, 0x3fb8aa3b, v125
	v_exp_f32_e32 v126, v126
	v_cmp_lt_f32_e32 vcc, 0, v125
	v_mul_f32_e32 v125, 0x3f867d5f, v125
	v_fma_f32 v126, v126, v72, v73
	s_nop 0
	v_cndmask_b32_e32 v125, v126, v125, vcc
	s_mov_b64 s[16:17], exec
	s_mov_b64 exec, s[30:31]
	global_store_dword v124, v125, s[26:27] offset:4
	s_mov_b64 exec, s[16:17]
